# K3 fast path (copy depth 8) + slow path: software-pipelined exact refine loop, write-through publish instead of L2 writeback fence
# speedup vs baseline: 1.0091x; 1.0017x over previous
_Z20refine_gather_kernelPKfS0_S0_S0_S0_S0_S0_PfPiS1_:
	s_load_dwordx16 s[4:19], s[0:1], 0x0
	s_load_dwordx4 s[20:23], s[0:1], 0x40
	v_and_b32_e32 v1, 63, v0
	s_bfe_u32 s24, s2, 0x30003
	s_lshr_b32 s25, s2, 6
	s_lshl_b32 s25, s25, 2
	s_bfe_u32 s26, s2, 0x20001
	s_or_b32 s25, s25, s26
	s_and_b32 s26, s2, 1
	v_lshlrev_b32_e32 v2, 5, v1
	v_lshl_or_b32 v2, s24, 11, v2
	s_waitcnt lgkmcnt(0)
	s_load_dword s27, s[14:15], 0x0
	global_load_dwordx4 v[4:7], v2, s[16:17]
	global_load_dwordx4 v[8:11], v2, s[16:17] offset:16
	s_cmp_eq_u32 s26, 0
	s_cselect_b32 s30, s4, s6
	s_cselect_b32 s31, s5, s7
	s_lshl_b32 s32, s24, 5
	s_add_i32 s32, s32, s25
	s_lshl_b32 s32, s32, 18
	s_lshl_b32 s33, s26, 26
	s_or_b32 s32, s32, s33
	s_add_u32 s34, s22, s32
	s_addc_u32 s35, s23, 0
	v_mov_b32_e32 v18, 0
	v_mov_b32_e32 v19, 0x7f800000
	s_waitcnt vmcnt(0) lgkmcnt(0)
	v_add_f32_e32 v12, v4, v5
	v_add_f32_e32 v13, v6, v7
	v_add_f32_e32 v14, v8, v9
	v_add_f32_e32 v15, v10, v11
	v_add_f32_e32 v12, v12, v13
	v_add_f32_e32 v14, v14, v15
	v_add_f32_e32 v12, v12, v14
	v_mov_b32_e32 v3, s27
	v_fmamk_f32 v3, v12, 0x3c800000, v3
	v_add_f32_e32 v16, 0xba03126f, v3
	v_add_f32_e32 v17, 0x3a03126f, v3
	v_readlane_b32 s40, v3, 0
	v_readlane_b32 s41, v3, 1
	v_readlane_b32 s42, v3, 2
	v_readlane_b32 s43, v3, 3
	v_readlane_b32 s44, v3, 4
	v_readlane_b32 s45, v3, 5
	v_readlane_b32 s46, v3, 6
	v_readlane_b32 s47, v3, 7
	v_cmp_gt_f32_e64 s[48:49], s40, v3
	v_cmp_gt_f32_e64 s[50:51], s41, v3
	v_cmp_gt_f32_e64 s[52:53], s42, v3
	v_cmp_gt_f32_e64 s[54:55], s43, v3
	v_cmp_gt_f32_e64 s[56:57], s44, v3
	v_cmp_gt_f32_e64 s[58:59], s45, v3
	v_cmp_gt_f32_e64 s[60:61], s46, v3
	v_cmp_gt_f32_e64 s[62:63], s47, v3
	v_addc_co_u32_e64 v18, vcc, 0, v18, s[48:49]
	v_addc_co_u32_e64 v18, vcc, 0, v18, s[50:51]
	v_addc_co_u32_e64 v18, vcc, 0, v18, s[52:53]
	v_addc_co_u32_e64 v18, vcc, 0, v18, s[54:55]
	v_addc_co_u32_e64 v18, vcc, 0, v18, s[56:57]
	v_addc_co_u32_e64 v18, vcc, 0, v18, s[58:59]
	v_addc_co_u32_e64 v18, vcc, 0, v18, s[60:61]
	v_addc_co_u32_e64 v18, vcc, 0, v18, s[62:63]
	v_readlane_b32 s40, v3, 8
	v_readlane_b32 s41, v3, 9
	v_readlane_b32 s42, v3, 10
	v_readlane_b32 s43, v3, 11
	v_readlane_b32 s44, v3, 12
	v_readlane_b32 s45, v3, 13
	v_readlane_b32 s46, v3, 14
	v_readlane_b32 s47, v3, 15
	v_cmp_gt_f32_e64 s[48:49], s40, v3
	v_cmp_gt_f32_e64 s[50:51], s41, v3
	v_cmp_gt_f32_e64 s[52:53], s42, v3
	v_cmp_gt_f32_e64 s[54:55], s43, v3
	v_cmp_gt_f32_e64 s[56:57], s44, v3
	v_cmp_gt_f32_e64 s[58:59], s45, v3
	v_cmp_gt_f32_e64 s[60:61], s46, v3
	v_cmp_gt_f32_e64 s[62:63], s47, v3
	v_addc_co_u32_e64 v18, vcc, 0, v18, s[48:49]
	v_addc_co_u32_e64 v18, vcc, 0, v18, s[50:51]
	v_addc_co_u32_e64 v18, vcc, 0, v18, s[52:53]
	v_addc_co_u32_e64 v18, vcc, 0, v18, s[54:55]
	v_addc_co_u32_e64 v18, vcc, 0, v18, s[56:57]
	v_addc_co_u32_e64 v18, vcc, 0, v18, s[58:59]
	v_addc_co_u32_e64 v18, vcc, 0, v18, s[60:61]
	v_addc_co_u32_e64 v18, vcc, 0, v18, s[62:63]
	v_readlane_b32 s40, v3, 16
	v_readlane_b32 s41, v3, 17
	v_readlane_b32 s42, v3, 18
	v_readlane_b32 s43, v3, 19
	v_readlane_b32 s44, v3, 20
	v_readlane_b32 s45, v3, 21
	v_readlane_b32 s46, v3, 22
	v_readlane_b32 s47, v3, 23
	v_cmp_gt_f32_e64 s[48:49], s40, v3
	v_cmp_gt_f32_e64 s[50:51], s41, v3
	v_cmp_gt_f32_e64 s[52:53], s42, v3
	v_cmp_gt_f32_e64 s[54:55], s43, v3
	v_cmp_gt_f32_e64 s[56:57], s44, v3
	v_cmp_gt_f32_e64 s[58:59], s45, v3
	v_cmp_gt_f32_e64 s[60:61], s46, v3
	v_cmp_gt_f32_e64 s[62:63], s47, v3
	v_addc_co_u32_e64 v18, vcc, 0, v18, s[48:49]
	v_addc_co_u32_e64 v18, vcc, 0, v18, s[50:51]
	v_addc_co_u32_e64 v18, vcc, 0, v18, s[52:53]
	v_addc_co_u32_e64 v18, vcc, 0, v18, s[54:55]
	v_addc_co_u32_e64 v18, vcc, 0, v18, s[56:57]
	v_addc_co_u32_e64 v18, vcc, 0, v18, s[58:59]
	v_addc_co_u32_e64 v18, vcc, 0, v18, s[60:61]
	v_addc_co_u32_e64 v18, vcc, 0, v18, s[62:63]
	v_readlane_b32 s40, v3, 24
	v_readlane_b32 s41, v3, 25
	v_readlane_b32 s42, v3, 26
	v_readlane_b32 s43, v3, 27
	v_readlane_b32 s44, v3, 28
	v_readlane_b32 s45, v3, 29
	v_readlane_b32 s46, v3, 30
	v_readlane_b32 s47, v3, 31
	v_cmp_gt_f32_e64 s[48:49], s40, v3
	v_cmp_gt_f32_e64 s[50:51], s41, v3
	v_cmp_gt_f32_e64 s[52:53], s42, v3
	v_cmp_gt_f32_e64 s[54:55], s43, v3
	v_cmp_gt_f32_e64 s[56:57], s44, v3
	v_cmp_gt_f32_e64 s[58:59], s45, v3
	v_cmp_gt_f32_e64 s[60:61], s46, v3
	v_cmp_gt_f32_e64 s[62:63], s47, v3
	v_addc_co_u32_e64 v18, vcc, 0, v18, s[48:49]
	v_addc_co_u32_e64 v18, vcc, 0, v18, s[50:51]
	v_addc_co_u32_e64 v18, vcc, 0, v18, s[52:53]
	v_addc_co_u32_e64 v18, vcc, 0, v18, s[54:55]
	v_addc_co_u32_e64 v18, vcc, 0, v18, s[56:57]
	v_addc_co_u32_e64 v18, vcc, 0, v18, s[58:59]
	v_addc_co_u32_e64 v18, vcc, 0, v18, s[60:61]
	v_addc_co_u32_e64 v18, vcc, 0, v18, s[62:63]
	v_readlane_b32 s40, v3, 32
	v_readlane_b32 s41, v3, 33
	v_readlane_b32 s42, v3, 34
	v_readlane_b32 s43, v3, 35
	v_readlane_b32 s44, v3, 36
	v_readlane_b32 s45, v3, 37
	v_readlane_b32 s46, v3, 38
	v_readlane_b32 s47, v3, 39
	v_cmp_gt_f32_e64 s[48:49], s40, v3
	v_cmp_gt_f32_e64 s[50:51], s41, v3
	v_cmp_gt_f32_e64 s[52:53], s42, v3
	v_cmp_gt_f32_e64 s[54:55], s43, v3
	v_cmp_gt_f32_e64 s[56:57], s44, v3
	v_cmp_gt_f32_e64 s[58:59], s45, v3
	v_cmp_gt_f32_e64 s[60:61], s46, v3
	v_cmp_gt_f32_e64 s[62:63], s47, v3
	v_addc_co_u32_e64 v18, vcc, 0, v18, s[48:49]
	v_addc_co_u32_e64 v18, vcc, 0, v18, s[50:51]
	v_addc_co_u32_e64 v18, vcc, 0, v18, s[52:53]
	v_addc_co_u32_e64 v18, vcc, 0, v18, s[54:55]
	v_addc_co_u32_e64 v18, vcc, 0, v18, s[56:57]
	v_addc_co_u32_e64 v18, vcc, 0, v18, s[58:59]
	v_addc_co_u32_e64 v18, vcc, 0, v18, s[60:61]
	v_addc_co_u32_e64 v18, vcc, 0, v18, s[62:63]
	v_readlane_b32 s40, v3, 40
	v_readlane_b32 s41, v3, 41
	v_readlane_b32 s42, v3, 42
	v_readlane_b32 s43, v3, 43
	v_readlane_b32 s44, v3, 44
	v_readlane_b32 s45, v3, 45
	v_readlane_b32 s46, v3, 46
	v_readlane_b32 s47, v3, 47
	v_cmp_gt_f32_e64 s[48:49], s40, v3
	v_cmp_gt_f32_e64 s[50:51], s41, v3
	v_cmp_gt_f32_e64 s[52:53], s42, v3
	v_cmp_gt_f32_e64 s[54:55], s43, v3
	v_cmp_gt_f32_e64 s[56:57], s44, v3
	v_cmp_gt_f32_e64 s[58:59], s45, v3
	v_cmp_gt_f32_e64 s[60:61], s46, v3
	v_cmp_gt_f32_e64 s[62:63], s47, v3
	v_addc_co_u32_e64 v18, vcc, 0, v18, s[48:49]
	v_addc_co_u32_e64 v18, vcc, 0, v18, s[50:51]
	v_addc_co_u32_e64 v18, vcc, 0, v18, s[52:53]
	v_addc_co_u32_e64 v18, vcc, 0, v18, s[54:55]
	v_addc_co_u32_e64 v18, vcc, 0, v18, s[56:57]
	v_addc_co_u32_e64 v18, vcc, 0, v18, s[58:59]
	v_addc_co_u32_e64 v18, vcc, 0, v18, s[60:61]
	v_addc_co_u32_e64 v18, vcc, 0, v18, s[62:63]
	v_readlane_b32 s40, v3, 48
	v_readlane_b32 s41, v3, 49
	v_readlane_b32 s42, v3, 50
	v_readlane_b32 s43, v3, 51
	v_readlane_b32 s44, v3, 52
	v_readlane_b32 s45, v3, 53
	v_readlane_b32 s46, v3, 54
	v_readlane_b32 s47, v3, 55
	v_cmp_gt_f32_e64 s[48:49], s40, v3
	v_cmp_gt_f32_e64 s[50:51], s41, v3
	v_cmp_gt_f32_e64 s[52:53], s42, v3
	v_cmp_gt_f32_e64 s[54:55], s43, v3
	v_cmp_gt_f32_e64 s[56:57], s44, v3
	v_cmp_gt_f32_e64 s[58:59], s45, v3
	v_cmp_gt_f32_e64 s[60:61], s46, v3
	v_cmp_gt_f32_e64 s[62:63], s47, v3
	v_addc_co_u32_e64 v18, vcc, 0, v18, s[48:49]
	v_addc_co_u32_e64 v18, vcc, 0, v18, s[50:51]
	v_addc_co_u32_e64 v18, vcc, 0, v18, s[52:53]
	v_addc_co_u32_e64 v18, vcc, 0, v18, s[54:55]
	v_addc_co_u32_e64 v18, vcc, 0, v18, s[56:57]
	v_addc_co_u32_e64 v18, vcc, 0, v18, s[58:59]
	v_addc_co_u32_e64 v18, vcc, 0, v18, s[60:61]
	v_addc_co_u32_e64 v18, vcc, 0, v18, s[62:63]
	v_readlane_b32 s40, v3, 56
	v_readlane_b32 s41, v3, 57
	v_readlane_b32 s42, v3, 58
	v_readlane_b32 s43, v3, 59
	v_readlane_b32 s44, v3, 60
	v_readlane_b32 s45, v3, 61
	v_readlane_b32 s46, v3, 62
	v_readlane_b32 s47, v3, 63
	v_cmp_gt_f32_e64 s[48:49], s40, v3
	v_cmp_gt_f32_e64 s[50:51], s41, v3
	v_cmp_gt_f32_e64 s[52:53], s42, v3
	v_cmp_gt_f32_e64 s[54:55], s43, v3
	v_cmp_gt_f32_e64 s[56:57], s44, v3
	v_cmp_gt_f32_e64 s[58:59], s45, v3
	v_cmp_gt_f32_e64 s[60:61], s46, v3
	v_cmp_gt_f32_e64 s[62:63], s47, v3
	v_addc_co_u32_e64 v18, vcc, 0, v18, s[48:49]
	v_addc_co_u32_e64 v18, vcc, 0, v18, s[50:51]
	v_addc_co_u32_e64 v18, vcc, 0, v18, s[52:53]
	v_addc_co_u32_e64 v18, vcc, 0, v18, s[54:55]
	v_addc_co_u32_e64 v18, vcc, 0, v18, s[56:57]
	v_addc_co_u32_e64 v18, vcc, 0, v18, s[58:59]
	v_addc_co_u32_e64 v18, vcc, 0, v18, s[60:61]
	v_addc_co_u32_e64 v18, vcc, 0, v18, s[62:63]
	v_cmp_gt_u32_e64 s[48:49], 32, v18
	v_cmp_gt_u32_e64 s[50:51], 33, v18
	s_nop 1
	v_cndmask_b32_e64 v20, v19, v3, s[48:49]
	v_cndmask_b32_e64 v21, v19, v3, s[50:51]
	s_nop 1
	v_min_f32_dpp v20, v20, v20 quad_perm:[1,0,3,2] row_mask:0xf bank_mask:0xf
	v_min_f32_dpp v21, v21, v21 quad_perm:[1,0,3,2] row_mask:0xf bank_mask:0xf
	s_nop 1
	v_min_f32_dpp v20, v20, v20 quad_perm:[2,3,0,1] row_mask:0xf bank_mask:0xf
	v_min_f32_dpp v21, v21, v21 quad_perm:[2,3,0,1] row_mask:0xf bank_mask:0xf
	s_nop 1
	v_min_f32_dpp v20, v20, v20 row_half_mirror row_mask:0xf bank_mask:0xf
	v_min_f32_dpp v21, v21, v21 row_half_mirror row_mask:0xf bank_mask:0xf
	s_nop 1
	v_min_f32_dpp v20, v20, v20 row_mirror row_mask:0xf bank_mask:0xf
	v_min_f32_dpp v21, v21, v21 row_mirror row_mask:0xf bank_mask:0xf
	s_nop 1
	v_readlane_b32 s40, v20, 0
	v_readlane_b32 s41, v20, 16
	v_readlane_b32 s42, v20, 32
	v_readlane_b32 s43, v20, 48
	v_readlane_b32 s44, v21, 0
	v_readlane_b32 s45, v21, 16
	v_readlane_b32 s46, v21, 32
	v_readlane_b32 s47, v21, 48
	v_mov_b32_e32 v22, s40
	v_mov_b32_e32 v23, s44
	v_min_f32_e32 v22, s41, v22
	v_min_f32_e32 v23, s45, v23
	v_min_f32_e32 v22, s42, v22
	v_min_f32_e32 v23, s46, v23
	v_min_f32_e32 v22, s43, v22
	v_min_f32_e32 v23, s47, v23
	v_cmp_lt_f32_e64 s[50:51], v23, v16
	v_cmp_gt_f32_e64 s[52:53], v22, v17
	s_or_b64 s[54:55], s[50:51], s[52:53]
	s_not_b64 s[54:55], s[54:55]
	s_cbranch_scc1 .Lrg_slow
	v_mbcnt_lo_u32_b32 v22, s50, 0
	v_mbcnt_hi_u32_b32 v22, s51, v22
	v_cmp_eq_u32_e64 s[56:57], s25, v22
	s_and_b64 s[56:57], s[56:57], s[50:51]
	s_ff1_i32_b64 s28, s[56:57]
	s_lshl_b32 s29, s24, 6
	s_add_i32 s29, s29, s28
	s_lshl_b32 s29, s29, 18
	s_add_u32 s30, s30, s29
	s_addc_u32 s31, s31, 0
	v_lshlrev_b32_e32 v2, 4, v0
	global_load_dwordx4 v[4:7], v2, s[30:31] nt
	s_add_u32 s30, s30, 0x1000
	s_addc_u32 s31, s31, 0
	global_load_dwordx4 v[8:11], v2, s[30:31] nt
	s_add_u32 s30, s30, 0x1000
	s_addc_u32 s31, s31, 0
	global_load_dwordx4 v[12:15], v2, s[30:31] nt
	s_add_u32 s30, s30, 0x1000
	s_addc_u32 s31, s31, 0
	global_load_dwordx4 v[16:19], v2, s[30:31] nt
	s_add_u32 s30, s30, 0x1000
	s_addc_u32 s31, s31, 0
	global_load_dwordx4 v[20:23], v2, s[30:31] nt
	s_add_u32 s30, s30, 0x1000
	s_addc_u32 s31, s31, 0
	global_load_dwordx4 v[24:27], v2, s[30:31] nt
	s_add_u32 s30, s30, 0x1000
	s_addc_u32 s31, s31, 0
	global_load_dwordx4 v[28:31], v2, s[30:31] nt
	s_add_u32 s30, s30, 0x1000
	s_addc_u32 s31, s31, 0
	global_load_dwordx4 v[32:35], v2, s[30:31] nt
	s_add_u32 s30, s30, 0x1000
	s_addc_u32 s31, s31, 0
	s_waitcnt vmcnt(7)
	global_store_dwordx4 v2, v[4:7], s[34:35] nt
	s_add_u32 s34, s34, 0x1000
	s_addc_u32 s35, s35, 0
	global_load_dwordx4 v[4:7], v2, s[30:31] nt
	s_add_u32 s30, s30, 0x1000
	s_addc_u32 s31, s31, 0
	s_waitcnt vmcnt(8)
	global_store_dwordx4 v2, v[8:11], s[34:35] nt
	s_add_u32 s34, s34, 0x1000
	s_addc_u32 s35, s35, 0
	global_load_dwordx4 v[8:11], v2, s[30:31] nt
	s_add_u32 s30, s30, 0x1000
	s_addc_u32 s31, s31, 0
	s_waitcnt vmcnt(9)
	global_store_dwordx4 v2, v[12:15], s[34:35] nt
	s_add_u32 s34, s34, 0x1000
	s_addc_u32 s35, s35, 0
	global_load_dwordx4 v[12:15], v2, s[30:31] nt
	s_add_u32 s30, s30, 0x1000
	s_addc_u32 s31, s31, 0
	s_waitcnt vmcnt(10)
	global_store_dwordx4 v2, v[16:19], s[34:35] nt
	s_add_u32 s34, s34, 0x1000
	s_addc_u32 s35, s35, 0
	global_load_dwordx4 v[16:19], v2, s[30:31] nt
	s_add_u32 s30, s30, 0x1000
	s_addc_u32 s31, s31, 0
	s_waitcnt vmcnt(11)
	global_store_dwordx4 v2, v[20:23], s[34:35] nt
	s_add_u32 s34, s34, 0x1000
	s_addc_u32 s35, s35, 0
	global_load_dwordx4 v[20:23], v2, s[30:31] nt
	s_add_u32 s30, s30, 0x1000
	s_addc_u32 s31, s31, 0
	s_waitcnt vmcnt(12)
	global_store_dwordx4 v2, v[24:27], s[34:35] nt
	s_add_u32 s34, s34, 0x1000
	s_addc_u32 s35, s35, 0
	global_load_dwordx4 v[24:27], v2, s[30:31] nt
	s_add_u32 s30, s30, 0x1000
	s_addc_u32 s31, s31, 0
	s_waitcnt vmcnt(13)
	global_store_dwordx4 v2, v[28:31], s[34:35] nt
	s_add_u32 s34, s34, 0x1000
	s_addc_u32 s35, s35, 0
	global_load_dwordx4 v[28:31], v2, s[30:31] nt
	s_add_u32 s30, s30, 0x1000
	s_addc_u32 s31, s31, 0
	s_waitcnt vmcnt(14)
	global_store_dwordx4 v2, v[32:35], s[34:35] nt
	s_add_u32 s34, s34, 0x1000
	s_addc_u32 s35, s35, 0
	global_load_dwordx4 v[32:35], v2, s[30:31] nt
	s_add_u32 s30, s30, 0x1000
	s_addc_u32 s31, s31, 0
	s_waitcnt vmcnt(14)
	global_store_dwordx4 v2, v[4:7], s[34:35] nt
	s_add_u32 s34, s34, 0x1000
	s_addc_u32 s35, s35, 0
	global_load_dwordx4 v[4:7], v2, s[30:31] nt
	s_add_u32 s30, s30, 0x1000
	s_addc_u32 s31, s31, 0
	s_waitcnt vmcnt(14)
	global_store_dwordx4 v2, v[8:11], s[34:35] nt
	s_add_u32 s34, s34, 0x1000
	s_addc_u32 s35, s35, 0
	global_load_dwordx4 v[8:11], v2, s[30:31] nt
	s_add_u32 s30, s30, 0x1000
	s_addc_u32 s31, s31, 0
	s_waitcnt vmcnt(14)
	global_store_dwordx4 v2, v[12:15], s[34:35] nt
	s_add_u32 s34, s34, 0x1000
	s_addc_u32 s35, s35, 0
	global_load_dwordx4 v[12:15], v2, s[30:31] nt
	s_add_u32 s30, s30, 0x1000
	s_addc_u32 s31, s31, 0
	s_waitcnt vmcnt(14)
	global_store_dwordx4 v2, v[16:19], s[34:35] nt
	s_add_u32 s34, s34, 0x1000
	s_addc_u32 s35, s35, 0
	global_load_dwordx4 v[16:19], v2, s[30:31] nt
	s_add_u32 s30, s30, 0x1000
	s_addc_u32 s31, s31, 0
	s_waitcnt vmcnt(14)
	global_store_dwordx4 v2, v[20:23], s[34:35] nt
	s_add_u32 s34, s34, 0x1000
	s_addc_u32 s35, s35, 0
	global_load_dwordx4 v[20:23], v2, s[30:31] nt
	s_add_u32 s30, s30, 0x1000
	s_addc_u32 s31, s31, 0
	s_waitcnt vmcnt(14)
	global_store_dwordx4 v2, v[24:27], s[34:35] nt
	s_add_u32 s34, s34, 0x1000
	s_addc_u32 s35, s35, 0
	global_load_dwordx4 v[24:27], v2, s[30:31] nt
	s_add_u32 s30, s30, 0x1000
	s_addc_u32 s31, s31, 0
	s_waitcnt vmcnt(14)
	global_store_dwordx4 v2, v[28:31], s[34:35] nt
	s_add_u32 s34, s34, 0x1000
	s_addc_u32 s35, s35, 0
	global_load_dwordx4 v[28:31], v2, s[30:31] nt
	s_add_u32 s30, s30, 0x1000
	s_addc_u32 s31, s31, 0
	s_waitcnt vmcnt(14)
	global_store_dwordx4 v2, v[32:35], s[34:35] nt
	s_add_u32 s34, s34, 0x1000
	s_addc_u32 s35, s35, 0
	global_load_dwordx4 v[32:35], v2, s[30:31] nt
	s_add_u32 s30, s30, 0x1000
	s_addc_u32 s31, s31, 0
	s_waitcnt vmcnt(14)
	global_store_dwordx4 v2, v[4:7], s[34:35] nt
	s_add_u32 s34, s34, 0x1000
	s_addc_u32 s35, s35, 0
	global_load_dwordx4 v[4:7], v2, s[30:31] nt
	s_add_u32 s30, s30, 0x1000
	s_addc_u32 s31, s31, 0
	s_waitcnt vmcnt(14)
	global_store_dwordx4 v2, v[8:11], s[34:35] nt
	s_add_u32 s34, s34, 0x1000
	s_addc_u32 s35, s35, 0
	global_load_dwordx4 v[8:11], v2, s[30:31] nt
	s_add_u32 s30, s30, 0x1000
	s_addc_u32 s31, s31, 0
	s_waitcnt vmcnt(14)
	global_store_dwordx4 v2, v[12:15], s[34:35] nt
	s_add_u32 s34, s34, 0x1000
	s_addc_u32 s35, s35, 0
	global_load_dwordx4 v[12:15], v2, s[30:31] nt
	s_add_u32 s30, s30, 0x1000
	s_addc_u32 s31, s31, 0
	s_waitcnt vmcnt(14)
	global_store_dwordx4 v2, v[16:19], s[34:35] nt
	s_add_u32 s34, s34, 0x1000
	s_addc_u32 s35, s35, 0
	global_load_dwordx4 v[16:19], v2, s[30:31] nt
	s_add_u32 s30, s30, 0x1000
	s_addc_u32 s31, s31, 0
	s_waitcnt vmcnt(14)
	global_store_dwordx4 v2, v[20:23], s[34:35] nt
	s_add_u32 s34, s34, 0x1000
	s_addc_u32 s35, s35, 0
	global_load_dwordx4 v[20:23], v2, s[30:31] nt
	s_add_u32 s30, s30, 0x1000
	s_addc_u32 s31, s31, 0
	s_waitcnt vmcnt(14)
	global_store_dwordx4 v2, v[24:27], s[34:35] nt
	s_add_u32 s34, s34, 0x1000
	s_addc_u32 s35, s35, 0
	global_load_dwordx4 v[24:27], v2, s[30:31] nt
	s_add_u32 s30, s30, 0x1000
	s_addc_u32 s31, s31, 0
	s_waitcnt vmcnt(14)
	global_store_dwordx4 v2, v[28:31], s[34:35] nt
	s_add_u32 s34, s34, 0x1000
	s_addc_u32 s35, s35, 0
	global_load_dwordx4 v[28:31], v2, s[30:31] nt
	s_add_u32 s30, s30, 0x1000
	s_addc_u32 s31, s31, 0
	s_waitcnt vmcnt(14)
	global_store_dwordx4 v2, v[32:35], s[34:35] nt
	s_add_u32 s34, s34, 0x1000
	s_addc_u32 s35, s35, 0
	global_load_dwordx4 v[32:35], v2, s[30:31] nt
	s_add_u32 s30, s30, 0x1000
	s_addc_u32 s31, s31, 0
	s_waitcnt vmcnt(14)
	global_store_dwordx4 v2, v[4:7], s[34:35] nt
	s_add_u32 s34, s34, 0x1000
	s_addc_u32 s35, s35, 0
	global_load_dwordx4 v[4:7], v2, s[30:31] nt
	s_add_u32 s30, s30, 0x1000
	s_addc_u32 s31, s31, 0
	s_waitcnt vmcnt(14)
	global_store_dwordx4 v2, v[8:11], s[34:35] nt
	s_add_u32 s34, s34, 0x1000
	s_addc_u32 s35, s35, 0
	global_load_dwordx4 v[8:11], v2, s[30:31] nt
	s_add_u32 s30, s30, 0x1000
	s_addc_u32 s31, s31, 0
	s_waitcnt vmcnt(14)
	global_store_dwordx4 v2, v[12:15], s[34:35] nt
	s_add_u32 s34, s34, 0x1000
	s_addc_u32 s35, s35, 0
	global_load_dwordx4 v[12:15], v2, s[30:31] nt
	s_add_u32 s30, s30, 0x1000
	s_addc_u32 s31, s31, 0
	s_waitcnt vmcnt(14)
	global_store_dwordx4 v2, v[16:19], s[34:35] nt
	s_add_u32 s34, s34, 0x1000
	s_addc_u32 s35, s35, 0
	global_load_dwordx4 v[16:19], v2, s[30:31] nt
	s_add_u32 s30, s30, 0x1000
	s_addc_u32 s31, s31, 0
	s_waitcnt vmcnt(14)
	global_store_dwordx4 v2, v[20:23], s[34:35] nt
	s_add_u32 s34, s34, 0x1000
	s_addc_u32 s35, s35, 0
	global_load_dwordx4 v[20:23], v2, s[30:31] nt
	s_add_u32 s30, s30, 0x1000
	s_addc_u32 s31, s31, 0
	s_waitcnt vmcnt(14)
	global_store_dwordx4 v2, v[24:27], s[34:35] nt
	s_add_u32 s34, s34, 0x1000
	s_addc_u32 s35, s35, 0
	global_load_dwordx4 v[24:27], v2, s[30:31] nt
	s_add_u32 s30, s30, 0x1000
	s_addc_u32 s31, s31, 0
	s_waitcnt vmcnt(14)
	global_store_dwordx4 v2, v[28:31], s[34:35] nt
	s_add_u32 s34, s34, 0x1000
	s_addc_u32 s35, s35, 0
	global_load_dwordx4 v[28:31], v2, s[30:31] nt
	s_add_u32 s30, s30, 0x1000
	s_addc_u32 s31, s31, 0
	s_waitcnt vmcnt(14)
	global_store_dwordx4 v2, v[32:35], s[34:35] nt
	s_add_u32 s34, s34, 0x1000
	s_addc_u32 s35, s35, 0
	global_load_dwordx4 v[32:35], v2, s[30:31] nt
	s_add_u32 s30, s30, 0x1000
	s_addc_u32 s31, s31, 0
	s_waitcnt vmcnt(14)
	global_store_dwordx4 v2, v[4:7], s[34:35] nt
	s_add_u32 s34, s34, 0x1000
	s_addc_u32 s35, s35, 0
	global_load_dwordx4 v[4:7], v2, s[30:31] nt
	s_add_u32 s30, s30, 0x1000
	s_addc_u32 s31, s31, 0
	s_waitcnt vmcnt(14)
	global_store_dwordx4 v2, v[8:11], s[34:35] nt
	s_add_u32 s34, s34, 0x1000
	s_addc_u32 s35, s35, 0
	global_load_dwordx4 v[8:11], v2, s[30:31] nt
	s_add_u32 s30, s30, 0x1000
	s_addc_u32 s31, s31, 0
	s_waitcnt vmcnt(14)
	global_store_dwordx4 v2, v[12:15], s[34:35] nt
	s_add_u32 s34, s34, 0x1000
	s_addc_u32 s35, s35, 0
	global_load_dwordx4 v[12:15], v2, s[30:31] nt
	s_add_u32 s30, s30, 0x1000
	s_addc_u32 s31, s31, 0
	s_waitcnt vmcnt(14)
	global_store_dwordx4 v2, v[16:19], s[34:35] nt
	s_add_u32 s34, s34, 0x1000
	s_addc_u32 s35, s35, 0
	global_load_dwordx4 v[16:19], v2, s[30:31] nt
	s_add_u32 s30, s30, 0x1000
	s_addc_u32 s31, s31, 0
	s_waitcnt vmcnt(14)
	global_store_dwordx4 v2, v[20:23], s[34:35] nt
	s_add_u32 s34, s34, 0x1000
	s_addc_u32 s35, s35, 0
	global_load_dwordx4 v[20:23], v2, s[30:31] nt
	s_add_u32 s30, s30, 0x1000
	s_addc_u32 s31, s31, 0
	s_waitcnt vmcnt(14)
	global_store_dwordx4 v2, v[24:27], s[34:35] nt
	s_add_u32 s34, s34, 0x1000
	s_addc_u32 s35, s35, 0
	global_load_dwordx4 v[24:27], v2, s[30:31] nt
	s_add_u32 s30, s30, 0x1000
	s_addc_u32 s31, s31, 0
	s_waitcnt vmcnt(14)
	global_store_dwordx4 v2, v[28:31], s[34:35] nt
	s_add_u32 s34, s34, 0x1000
	s_addc_u32 s35, s35, 0
	global_load_dwordx4 v[28:31], v2, s[30:31] nt
	s_add_u32 s30, s30, 0x1000
	s_addc_u32 s31, s31, 0
	s_waitcnt vmcnt(14)
	global_store_dwordx4 v2, v[32:35], s[34:35] nt
	s_add_u32 s34, s34, 0x1000
	s_addc_u32 s35, s35, 0
	global_load_dwordx4 v[32:35], v2, s[30:31] nt
	s_add_u32 s30, s30, 0x1000
	s_addc_u32 s31, s31, 0
	s_waitcnt vmcnt(14)
	global_store_dwordx4 v2, v[4:7], s[34:35] nt
	s_add_u32 s34, s34, 0x1000
	s_addc_u32 s35, s35, 0
	global_load_dwordx4 v[4:7], v2, s[30:31] nt
	s_add_u32 s30, s30, 0x1000
	s_addc_u32 s31, s31, 0
	s_waitcnt vmcnt(14)
	global_store_dwordx4 v2, v[8:11], s[34:35] nt
	s_add_u32 s34, s34, 0x1000
	s_addc_u32 s35, s35, 0
	global_load_dwordx4 v[8:11], v2, s[30:31] nt
	s_add_u32 s30, s30, 0x1000
	s_addc_u32 s31, s31, 0
	s_waitcnt vmcnt(14)
	global_store_dwordx4 v2, v[12:15], s[34:35] nt
	s_add_u32 s34, s34, 0x1000
	s_addc_u32 s35, s35, 0
	global_load_dwordx4 v[12:15], v2, s[30:31] nt
	s_add_u32 s30, s30, 0x1000
	s_addc_u32 s31, s31, 0
	s_waitcnt vmcnt(14)
	global_store_dwordx4 v2, v[16:19], s[34:35] nt
	s_add_u32 s34, s34, 0x1000
	s_addc_u32 s35, s35, 0
	global_load_dwordx4 v[16:19], v2, s[30:31] nt
	s_add_u32 s30, s30, 0x1000
	s_addc_u32 s31, s31, 0
	s_waitcnt vmcnt(14)
	global_store_dwordx4 v2, v[20:23], s[34:35] nt
	s_add_u32 s34, s34, 0x1000
	s_addc_u32 s35, s35, 0
	global_load_dwordx4 v[20:23], v2, s[30:31] nt
	s_add_u32 s30, s30, 0x1000
	s_addc_u32 s31, s31, 0
	s_waitcnt vmcnt(14)
	global_store_dwordx4 v2, v[24:27], s[34:35] nt
	s_add_u32 s34, s34, 0x1000
	s_addc_u32 s35, s35, 0
	global_load_dwordx4 v[24:27], v2, s[30:31] nt
	s_add_u32 s30, s30, 0x1000
	s_addc_u32 s31, s31, 0
	s_waitcnt vmcnt(14)
	global_store_dwordx4 v2, v[28:31], s[34:35] nt
	s_add_u32 s34, s34, 0x1000
	s_addc_u32 s35, s35, 0
	global_load_dwordx4 v[28:31], v2, s[30:31] nt
	s_add_u32 s30, s30, 0x1000
	s_addc_u32 s31, s31, 0
	s_waitcnt vmcnt(14)
	global_store_dwordx4 v2, v[32:35], s[34:35] nt
	s_add_u32 s34, s34, 0x1000
	s_addc_u32 s35, s35, 0
	global_load_dwordx4 v[32:35], v2, s[30:31] nt
	s_add_u32 s30, s30, 0x1000
	s_addc_u32 s31, s31, 0
	s_waitcnt vmcnt(14)
	global_store_dwordx4 v2, v[4:7], s[34:35] nt
	s_add_u32 s34, s34, 0x1000
	s_addc_u32 s35, s35, 0
	global_load_dwordx4 v[4:7], v2, s[30:31] nt
	s_add_u32 s30, s30, 0x1000
	s_addc_u32 s31, s31, 0
	s_waitcnt vmcnt(14)
	global_store_dwordx4 v2, v[8:11], s[34:35] nt
	s_add_u32 s34, s34, 0x1000
	s_addc_u32 s35, s35, 0
	global_load_dwordx4 v[8:11], v2, s[30:31] nt
	s_add_u32 s30, s30, 0x1000
	s_addc_u32 s31, s31, 0
	s_waitcnt vmcnt(14)
	global_store_dwordx4 v2, v[12:15], s[34:35] nt
	s_add_u32 s34, s34, 0x1000
	s_addc_u32 s35, s35, 0
	global_load_dwordx4 v[12:15], v2, s[30:31] nt
	s_add_u32 s30, s30, 0x1000
	s_addc_u32 s31, s31, 0
	s_waitcnt vmcnt(14)
	global_store_dwordx4 v2, v[16:19], s[34:35] nt
	s_add_u32 s34, s34, 0x1000
	s_addc_u32 s35, s35, 0
	global_load_dwordx4 v[16:19], v2, s[30:31] nt
	s_add_u32 s30, s30, 0x1000
	s_addc_u32 s31, s31, 0
	s_waitcnt vmcnt(14)
	global_store_dwordx4 v2, v[20:23], s[34:35] nt
	s_add_u32 s34, s34, 0x1000
	s_addc_u32 s35, s35, 0
	global_load_dwordx4 v[20:23], v2, s[30:31] nt
	s_add_u32 s30, s30, 0x1000
	s_addc_u32 s31, s31, 0
	s_waitcnt vmcnt(14)
	global_store_dwordx4 v2, v[24:27], s[34:35] nt
	s_add_u32 s34, s34, 0x1000
	s_addc_u32 s35, s35, 0
	global_load_dwordx4 v[24:27], v2, s[30:31] nt
	s_add_u32 s30, s30, 0x1000
	s_addc_u32 s31, s31, 0
	s_waitcnt vmcnt(14)
	global_store_dwordx4 v2, v[28:31], s[34:35] nt
	s_add_u32 s34, s34, 0x1000
	s_addc_u32 s35, s35, 0
	global_load_dwordx4 v[28:31], v2, s[30:31] nt
	s_add_u32 s30, s30, 0x1000
	s_addc_u32 s31, s31, 0
	s_waitcnt vmcnt(14)
	global_store_dwordx4 v2, v[32:35], s[34:35] nt
	s_add_u32 s34, s34, 0x1000
	s_addc_u32 s35, s35, 0
	global_load_dwordx4 v[32:35], v2, s[30:31] nt
	s_add_u32 s30, s30, 0x1000
	s_addc_u32 s31, s31, 0
	s_waitcnt vmcnt(14)
	global_store_dwordx4 v2, v[4:7], s[34:35] nt
	s_add_u32 s34, s34, 0x1000
	s_addc_u32 s35, s35, 0
	s_waitcnt vmcnt(13)
	global_store_dwordx4 v2, v[8:11], s[34:35] nt
	s_add_u32 s34, s34, 0x1000
	s_addc_u32 s35, s35, 0
	s_waitcnt vmcnt(12)
	global_store_dwordx4 v2, v[12:15], s[34:35] nt
	s_add_u32 s34, s34, 0x1000
	s_addc_u32 s35, s35, 0
	s_waitcnt vmcnt(11)
	global_store_dwordx4 v2, v[16:19], s[34:35] nt
	s_add_u32 s34, s34, 0x1000
	s_addc_u32 s35, s35, 0
	s_waitcnt vmcnt(10)
	global_store_dwordx4 v2, v[20:23], s[34:35] nt
	s_add_u32 s34, s34, 0x1000
	s_addc_u32 s35, s35, 0
	s_waitcnt vmcnt(9)
	global_store_dwordx4 v2, v[24:27], s[34:35] nt
	s_add_u32 s34, s34, 0x1000
	s_addc_u32 s35, s35, 0
	s_waitcnt vmcnt(8)
	global_store_dwordx4 v2, v[28:31], s[34:35] nt
	s_add_u32 s34, s34, 0x1000
	s_addc_u32 s35, s35, 0
	s_waitcnt vmcnt(7)
	global_store_dwordx4 v2, v[32:35], s[34:35] nt
	s_add_u32 s34, s34, 0x1000
	s_addc_u32 s35, s35, 0
	s_endpgm

.LBB2_14:
	s_and_b32 s28, s34, 15
	s_ff1_i32_b64 s37, s[30:31]
	s_lshl_b32 s28, s28, 7
	v_lshl_add_u64 v[14:15], v[4:5], 0, s[28:29]
	v_lshl_add_u64 v[16:17], v[6:7], 0, s[28:29]
	v_lshl_add_u64 v[18:19], v[8:9], 0, s[28:29]
	v_lshl_add_u64 v[20:21], v[10:11], 0, s[28:29]
	s_add_i32 s28, s39, s37
	s_lshl_b32 s30, s34, 1
	v_lshl_or_b32 v22, s28, 6, v2
	v_and_or_b32 v22, s30, 32, v22
	v_mov_b32_e32 v23, v1
	v_lshlrev_b64 v[24:25], 12, v[22:23]
	s_and_b32 s36, s34, 31
	v_lshl_add_u64 v[22:23], s[12:13], 0, v[24:25]
	v_lshl_add_u64 v[24:25], s[14:15], 0, v[24:25]
	v_accvgpr_write_b32 a15, 0
	v_accvgpr_write_b32 a14, 0
	v_accvgpr_write_b32 a13, 0
	v_accvgpr_write_b32 a12, 0
	v_accvgpr_write_b32 a11, 0
	v_accvgpr_write_b32 a10, 0
	v_accvgpr_write_b32 a9, 0
	v_accvgpr_write_b32 a8, 0
	v_accvgpr_write_b32 a7, 0
	v_accvgpr_write_b32 a6, 0
	v_accvgpr_write_b32 a5, 0
	v_accvgpr_write_b32 a4, 0
	v_accvgpr_write_b32 a3, 0
	v_accvgpr_write_b32 a2, 0
	v_accvgpr_write_b32 a1, 0
	v_accvgpr_write_b32 a0, 0
	s_mov_b64 s[30:31], 0
	v_lshl_add_u64 v[184:185], v[22:23], 0, v[12:13]
	v_lshl_add_u64 v[186:187], v[24:25], 0, v[12:13]
	s_mov_b32 s31, 0
	s_mov_b32 s30, 0x1000
	global_load_dwordx4 v[38:41], v[184:185], off offset:0
	global_load_dwordx4 v[54:57], v[186:187], off offset:0
	global_load_dwordx4 v[42:45], v[184:185], off offset:32
	global_load_dwordx4 v[58:61], v[186:187], off offset:32
	global_load_dwordx4 v[46:49], v[184:185], off offset:64
	global_load_dwordx4 v[62:65], v[186:187], off offset:64
	global_load_dwordx4 v[50:53], v[184:185], off offset:96
	global_load_dwordx4 v[66:69], v[186:187], off offset:96
	v_lshl_add_u64 v[188:189], v[16:17], 0, s[30:31]
	global_load_dword v70, v[188:189], off offset:-4096
	global_load_dword v71, v[188:189], off offset:-2048
	global_load_dword v72, v[188:189], off offset:0
	global_load_dword v73, v[188:189], off offset:2048
	v_lshl_add_u64 v[188:189], v[20:21], 0, s[30:31]
	global_load_dword v74, v[188:189], off offset:-4096
	global_load_dword v75, v[188:189], off offset:-2048
	global_load_dword v76, v[188:189], off offset:0
	global_load_dword v77, v[188:189], off offset:2048
	v_lshl_add_u64 v[188:189], v[18:19], 0, s[30:31]
	global_load_dword v78, v[188:189], off offset:-4096
	global_load_dword v79, v[188:189], off offset:-2048
	global_load_dword v80, v[188:189], off offset:0
	global_load_dword v81, v[188:189], off offset:2048
	v_lshl_add_u64 v[188:189], v[14:15], 0, s[30:31]
	global_load_dword v82, v[188:189], off offset:-4096
	global_load_dword v83, v[188:189], off offset:-2048
	global_load_dword v84, v[188:189], off offset:0
	global_load_dword v85, v[188:189], off offset:2048
	s_mov_b32 s30, 0x11000
	global_load_dwordx4 v[86:89], v[184:185], off offset:128
	global_load_dwordx4 v[102:105], v[186:187], off offset:128
	global_load_dwordx4 v[90:93], v[184:185], off offset:160
	global_load_dwordx4 v[106:109], v[186:187], off offset:160
	global_load_dwordx4 v[94:97], v[184:185], off offset:192
	global_load_dwordx4 v[110:113], v[186:187], off offset:192
	global_load_dwordx4 v[98:101], v[184:185], off offset:224
	global_load_dwordx4 v[114:117], v[186:187], off offset:224
	v_lshl_add_u64 v[188:189], v[16:17], 0, s[30:31]
	global_load_dword v118, v[188:189], off offset:-4096
	global_load_dword v119, v[188:189], off offset:-2048
	global_load_dword v120, v[188:189], off offset:0
	global_load_dword v121, v[188:189], off offset:2048
	v_lshl_add_u64 v[188:189], v[20:21], 0, s[30:31]
	global_load_dword v122, v[188:189], off offset:-4096
	global_load_dword v123, v[188:189], off offset:-2048
	global_load_dword v124, v[188:189], off offset:0
	global_load_dword v125, v[188:189], off offset:2048
	v_lshl_add_u64 v[188:189], v[18:19], 0, s[30:31]
	global_load_dword v126, v[188:189], off offset:-4096
	global_load_dword v127, v[188:189], off offset:-2048
	global_load_dword v128, v[188:189], off offset:0
	global_load_dword v129, v[188:189], off offset:2048
	v_lshl_add_u64 v[188:189], v[14:15], 0, s[30:31]
	global_load_dword v130, v[188:189], off offset:-4096
	global_load_dword v131, v[188:189], off offset:-2048
	global_load_dword v132, v[188:189], off offset:0
	global_load_dword v133, v[188:189], off offset:2048
	s_mov_b32 s30, 0x21000
	s_waitcnt vmcnt(46)
	v_add_f32_e32 v38, v38, v54
	v_mul_f32_e32 v38, 0.5, v38
	v_add_f32_e32 v39, v39, v55
	v_mul_f32_e32 v39, 0.5, v39
	v_add_f32_e32 v40, v40, v56
	v_mul_f32_e32 v40, 0.5, v40
	s_waitcnt vmcnt(39)
	v_mfma_f32_32x32x2_f32 a[0:15], v38, v70, a[0:15]
	global_load_dwordx4 v[134:137], v[184:185], off offset:256
	global_load_dwordx4 v[150:153], v[186:187], off offset:256
	v_add_f32_e32 v41, v41, v57
	v_mul_f32_e32 v41, 0.5, v41
	s_waitcnt vmcnt(40)
	v_mfma_f32_32x32x2_f32 a[0:15], v39, v71, a[0:15]
	global_load_dwordx4 v[138:141], v[184:185], off offset:288
	global_load_dwordx4 v[154:157], v[186:187], off offset:288
	v_add_f32_e32 v42, v42, v58
	v_mul_f32_e32 v42, 0.5, v42
	s_waitcnt vmcnt(41)
	v_mfma_f32_32x32x2_f32 a[0:15], v40, v72, a[0:15]
	global_load_dwordx4 v[142:145], v[184:185], off offset:320
	global_load_dwordx4 v[158:161], v[186:187], off offset:320
	v_add_f32_e32 v43, v43, v59
	v_mul_f32_e32 v43, 0.5, v43
	s_waitcnt vmcnt(42)
	v_mfma_f32_32x32x2_f32 a[0:15], v41, v73, a[0:15]
	global_load_dwordx4 v[146:149], v[184:185], off offset:352
	global_load_dwordx4 v[162:165], v[186:187], off offset:352
	v_add_f32_e32 v44, v44, v60
	v_mul_f32_e32 v44, 0.5, v44
	s_waitcnt vmcnt(43)
	v_mfma_f32_32x32x2_f32 a[0:15], v42, v74, a[0:15]
	v_lshl_add_u64 v[188:189], v[16:17], 0, s[30:31]
	global_load_dword v166, v[188:189], off offset:-4096
	global_load_dword v167, v[188:189], off offset:-2048
	v_add_f32_e32 v45, v45, v61
	v_mul_f32_e32 v45, 0.5, v45
	s_waitcnt vmcnt(44)
	v_mfma_f32_32x32x2_f32 a[0:15], v43, v75, a[0:15]
	global_load_dword v168, v[188:189], off offset:0
	global_load_dword v169, v[188:189], off offset:2048
	v_add_f32_e32 v46, v46, v62
	v_mul_f32_e32 v46, 0.5, v46
	s_waitcnt vmcnt(45)
	v_mfma_f32_32x32x2_f32 a[0:15], v44, v76, a[0:15]
	v_lshl_add_u64 v[188:189], v[20:21], 0, s[30:31]
	global_load_dword v170, v[188:189], off offset:-4096
	global_load_dword v171, v[188:189], off offset:-2048
	v_add_f32_e32 v47, v47, v63
	v_mul_f32_e32 v47, 0.5, v47
	s_waitcnt vmcnt(46)
	v_mfma_f32_32x32x2_f32 a[0:15], v45, v77, a[0:15]
	global_load_dword v172, v[188:189], off offset:0
	global_load_dword v173, v[188:189], off offset:2048
	v_add_f32_e32 v48, v48, v64
	v_mul_f32_e32 v48, 0.5, v48
	s_waitcnt vmcnt(47)
	v_mfma_f32_32x32x2_f32 a[0:15], v46, v78, a[0:15]
	v_lshl_add_u64 v[188:189], v[18:19], 0, s[30:31]
	global_load_dword v174, v[188:189], off offset:-4096
	global_load_dword v175, v[188:189], off offset:-2048
	v_add_f32_e32 v49, v49, v65
	v_mul_f32_e32 v49, 0.5, v49
	s_waitcnt vmcnt(48)
	v_mfma_f32_32x32x2_f32 a[0:15], v47, v79, a[0:15]
	global_load_dword v176, v[188:189], off offset:0
	global_load_dword v177, v[188:189], off offset:2048
	v_add_f32_e32 v50, v50, v66
	v_mul_f32_e32 v50, 0.5, v50
	s_waitcnt vmcnt(49)
	v_mfma_f32_32x32x2_f32 a[0:15], v48, v80, a[0:15]
	v_lshl_add_u64 v[188:189], v[14:15], 0, s[30:31]
	global_load_dword v178, v[188:189], off offset:-4096
	global_load_dword v179, v[188:189], off offset:-2048
	v_add_f32_e32 v51, v51, v67
	v_mul_f32_e32 v51, 0.5, v51
	s_waitcnt vmcnt(50)
	v_mfma_f32_32x32x2_f32 a[0:15], v49, v81, a[0:15]
	global_load_dword v180, v[188:189], off offset:0
	global_load_dword v181, v[188:189], off offset:2048
	v_add_f32_e32 v52, v52, v68
	v_mul_f32_e32 v52, 0.5, v52
	s_waitcnt vmcnt(51)
	v_mfma_f32_32x32x2_f32 a[0:15], v50, v82, a[0:15]
	v_add_f32_e32 v53, v53, v69
	v_mul_f32_e32 v53, 0.5, v53
	s_waitcnt vmcnt(50)
	v_mfma_f32_32x32x2_f32 a[0:15], v51, v83, a[0:15]
	s_waitcnt vmcnt(49)
	v_mfma_f32_32x32x2_f32 a[0:15], v52, v84, a[0:15]
	s_waitcnt vmcnt(48)
	v_mfma_f32_32x32x2_f32 a[0:15], v53, v85, a[0:15]
	s_mov_b32 s30, 0x31000
	s_waitcnt vmcnt(46)
	v_add_f32_e32 v86, v86, v102
	v_mul_f32_e32 v86, 0.5, v86
	v_add_f32_e32 v87, v87, v103
	v_mul_f32_e32 v87, 0.5, v87
	v_add_f32_e32 v88, v88, v104
	v_mul_f32_e32 v88, 0.5, v88
	s_waitcnt vmcnt(39)
	v_mfma_f32_32x32x2_f32 a[0:15], v86, v118, a[0:15]
	global_load_dwordx4 v[38:41], v[184:185], off offset:384
	global_load_dwordx4 v[54:57], v[186:187], off offset:384
	v_add_f32_e32 v89, v89, v105
	v_mul_f32_e32 v89, 0.5, v89
	s_waitcnt vmcnt(40)
	v_mfma_f32_32x32x2_f32 a[0:15], v87, v119, a[0:15]
	global_load_dwordx4 v[42:45], v[184:185], off offset:416
	global_load_dwordx4 v[58:61], v[186:187], off offset:416
	v_add_f32_e32 v90, v90, v106
	v_mul_f32_e32 v90, 0.5, v90
	s_waitcnt vmcnt(41)
	v_mfma_f32_32x32x2_f32 a[0:15], v88, v120, a[0:15]
	global_load_dwordx4 v[46:49], v[184:185], off offset:448
	global_load_dwordx4 v[62:65], v[186:187], off offset:448
	v_add_f32_e32 v91, v91, v107
	v_mul_f32_e32 v91, 0.5, v91
	s_waitcnt vmcnt(42)
	v_mfma_f32_32x32x2_f32 a[0:15], v89, v121, a[0:15]
	global_load_dwordx4 v[50:53], v[184:185], off offset:480
	global_load_dwordx4 v[66:69], v[186:187], off offset:480
	v_add_f32_e32 v92, v92, v108
	v_mul_f32_e32 v92, 0.5, v92
	s_waitcnt vmcnt(43)
	v_mfma_f32_32x32x2_f32 a[0:15], v90, v122, a[0:15]
	v_lshl_add_u64 v[188:189], v[16:17], 0, s[30:31]
	global_load_dword v70, v[188:189], off offset:-4096
	global_load_dword v71, v[188:189], off offset:-2048
	v_add_f32_e32 v93, v93, v109
	v_mul_f32_e32 v93, 0.5, v93
	s_waitcnt vmcnt(44)
	v_mfma_f32_32x32x2_f32 a[0:15], v91, v123, a[0:15]
	global_load_dword v72, v[188:189], off offset:0
	global_load_dword v73, v[188:189], off offset:2048
	v_add_f32_e32 v94, v94, v110
	v_mul_f32_e32 v94, 0.5, v94
	s_waitcnt vmcnt(45)
	v_mfma_f32_32x32x2_f32 a[0:15], v92, v124, a[0:15]
	v_lshl_add_u64 v[188:189], v[20:21], 0, s[30:31]
	global_load_dword v74, v[188:189], off offset:-4096
	global_load_dword v75, v[188:189], off offset:-2048
	v_add_f32_e32 v95, v95, v111
	v_mul_f32_e32 v95, 0.5, v95
	s_waitcnt vmcnt(46)
	v_mfma_f32_32x32x2_f32 a[0:15], v93, v125, a[0:15]
	global_load_dword v76, v[188:189], off offset:0
	global_load_dword v77, v[188:189], off offset:2048
	v_add_f32_e32 v96, v96, v112
	v_mul_f32_e32 v96, 0.5, v96
	s_waitcnt vmcnt(47)
	v_mfma_f32_32x32x2_f32 a[0:15], v94, v126, a[0:15]
	v_lshl_add_u64 v[188:189], v[18:19], 0, s[30:31]
	global_load_dword v78, v[188:189], off offset:-4096
	global_load_dword v79, v[188:189], off offset:-2048
	v_add_f32_e32 v97, v97, v113
	v_mul_f32_e32 v97, 0.5, v97
	s_waitcnt vmcnt(48)
	v_mfma_f32_32x32x2_f32 a[0:15], v95, v127, a[0:15]
	global_load_dword v80, v[188:189], off offset:0
	global_load_dword v81, v[188:189], off offset:2048
	v_add_f32_e32 v98, v98, v114
	v_mul_f32_e32 v98, 0.5, v98
	s_waitcnt vmcnt(49)
	v_mfma_f32_32x32x2_f32 a[0:15], v96, v128, a[0:15]
	v_lshl_add_u64 v[188:189], v[14:15], 0, s[30:31]
	global_load_dword v82, v[188:189], off offset:-4096
	global_load_dword v83, v[188:189], off offset:-2048
	v_add_f32_e32 v99, v99, v115
	v_mul_f32_e32 v99, 0.5, v99
	s_waitcnt vmcnt(50)
	v_mfma_f32_32x32x2_f32 a[0:15], v97, v129, a[0:15]
	global_load_dword v84, v[188:189], off offset:0
	global_load_dword v85, v[188:189], off offset:2048
	v_add_f32_e32 v100, v100, v116
	v_mul_f32_e32 v100, 0.5, v100
	s_waitcnt vmcnt(51)
	v_mfma_f32_32x32x2_f32 a[0:15], v98, v130, a[0:15]
	v_add_f32_e32 v101, v101, v117
	v_mul_f32_e32 v101, 0.5, v101
	s_waitcnt vmcnt(50)
	v_mfma_f32_32x32x2_f32 a[0:15], v99, v131, a[0:15]
	s_waitcnt vmcnt(49)
	v_mfma_f32_32x32x2_f32 a[0:15], v100, v132, a[0:15]
	s_waitcnt vmcnt(48)
	v_mfma_f32_32x32x2_f32 a[0:15], v101, v133, a[0:15]
	s_mov_b32 s30, 0x41000
	s_waitcnt vmcnt(46)
	v_add_f32_e32 v134, v134, v150
	v_mul_f32_e32 v134, 0.5, v134
	v_add_f32_e32 v135, v135, v151
	v_mul_f32_e32 v135, 0.5, v135
	v_add_f32_e32 v136, v136, v152
	v_mul_f32_e32 v136, 0.5, v136
	s_waitcnt vmcnt(39)
	v_mfma_f32_32x32x2_f32 a[0:15], v134, v166, a[0:15]
	global_load_dwordx4 v[86:89], v[184:185], off offset:512
	global_load_dwordx4 v[102:105], v[186:187], off offset:512
	v_add_f32_e32 v137, v137, v153
	v_mul_f32_e32 v137, 0.5, v137
	s_waitcnt vmcnt(40)
	v_mfma_f32_32x32x2_f32 a[0:15], v135, v167, a[0:15]
	global_load_dwordx4 v[90:93], v[184:185], off offset:544
	global_load_dwordx4 v[106:109], v[186:187], off offset:544
	v_add_f32_e32 v138, v138, v154
	v_mul_f32_e32 v138, 0.5, v138
	s_waitcnt vmcnt(41)
	v_mfma_f32_32x32x2_f32 a[0:15], v136, v168, a[0:15]
	global_load_dwordx4 v[94:97], v[184:185], off offset:576
	global_load_dwordx4 v[110:113], v[186:187], off offset:576
	v_add_f32_e32 v139, v139, v155
	v_mul_f32_e32 v139, 0.5, v139
	s_waitcnt vmcnt(42)
	v_mfma_f32_32x32x2_f32 a[0:15], v137, v169, a[0:15]
	global_load_dwordx4 v[98:101], v[184:185], off offset:608
	global_load_dwordx4 v[114:117], v[186:187], off offset:608
	v_add_f32_e32 v140, v140, v156
	v_mul_f32_e32 v140, 0.5, v140
	s_waitcnt vmcnt(43)
	v_mfma_f32_32x32x2_f32 a[0:15], v138, v170, a[0:15]
	v_lshl_add_u64 v[188:189], v[16:17], 0, s[30:31]
	global_load_dword v118, v[188:189], off offset:-4096
	global_load_dword v119, v[188:189], off offset:-2048
	v_add_f32_e32 v141, v141, v157
	v_mul_f32_e32 v141, 0.5, v141
	s_waitcnt vmcnt(44)
	v_mfma_f32_32x32x2_f32 a[0:15], v139, v171, a[0:15]
	global_load_dword v120, v[188:189], off offset:0
	global_load_dword v121, v[188:189], off offset:2048
	v_add_f32_e32 v142, v142, v158
	v_mul_f32_e32 v142, 0.5, v142
	s_waitcnt vmcnt(45)
	v_mfma_f32_32x32x2_f32 a[0:15], v140, v172, a[0:15]
	v_lshl_add_u64 v[188:189], v[20:21], 0, s[30:31]
	global_load_dword v122, v[188:189], off offset:-4096
	global_load_dword v123, v[188:189], off offset:-2048
	v_add_f32_e32 v143, v143, v159
	v_mul_f32_e32 v143, 0.5, v143
	s_waitcnt vmcnt(46)
	v_mfma_f32_32x32x2_f32 a[0:15], v141, v173, a[0:15]
	global_load_dword v124, v[188:189], off offset:0
	global_load_dword v125, v[188:189], off offset:2048
	v_add_f32_e32 v144, v144, v160
	v_mul_f32_e32 v144, 0.5, v144
	s_waitcnt vmcnt(47)
	v_mfma_f32_32x32x2_f32 a[0:15], v142, v174, a[0:15]
	v_lshl_add_u64 v[188:189], v[18:19], 0, s[30:31]
	global_load_dword v126, v[188:189], off offset:-4096
	global_load_dword v127, v[188:189], off offset:-2048
	v_add_f32_e32 v145, v145, v161
	v_mul_f32_e32 v145, 0.5, v145
	s_waitcnt vmcnt(48)
	v_mfma_f32_32x32x2_f32 a[0:15], v143, v175, a[0:15]
	global_load_dword v128, v[188:189], off offset:0
	global_load_dword v129, v[188:189], off offset:2048
	v_add_f32_e32 v146, v146, v162
	v_mul_f32_e32 v146, 0.5, v146
	s_waitcnt vmcnt(49)
	v_mfma_f32_32x32x2_f32 a[0:15], v144, v176, a[0:15]
	v_lshl_add_u64 v[188:189], v[14:15], 0, s[30:31]
	global_load_dword v130, v[188:189], off offset:-4096
	global_load_dword v131, v[188:189], off offset:-2048
	v_add_f32_e32 v147, v147, v163
	v_mul_f32_e32 v147, 0.5, v147
	s_waitcnt vmcnt(50)
	v_mfma_f32_32x32x2_f32 a[0:15], v145, v177, a[0:15]
	global_load_dword v132, v[188:189], off offset:0
	global_load_dword v133, v[188:189], off offset:2048
	v_add_f32_e32 v148, v148, v164
	v_mul_f32_e32 v148, 0.5, v148
	s_waitcnt vmcnt(51)
	v_mfma_f32_32x32x2_f32 a[0:15], v146, v178, a[0:15]
	v_add_f32_e32 v149, v149, v165
	v_mul_f32_e32 v149, 0.5, v149
	s_waitcnt vmcnt(50)
	v_mfma_f32_32x32x2_f32 a[0:15], v147, v179, a[0:15]
	s_waitcnt vmcnt(49)
	v_mfma_f32_32x32x2_f32 a[0:15], v148, v180, a[0:15]
	s_waitcnt vmcnt(48)
	v_mfma_f32_32x32x2_f32 a[0:15], v149, v181, a[0:15]
	s_mov_b32 s30, 0x51000
	s_waitcnt vmcnt(46)
	v_add_f32_e32 v38, v38, v54
	v_mul_f32_e32 v38, 0.5, v38
	v_add_f32_e32 v39, v39, v55
	v_mul_f32_e32 v39, 0.5, v39
	v_add_f32_e32 v40, v40, v56
	v_mul_f32_e32 v40, 0.5, v40
	s_waitcnt vmcnt(39)
	v_mfma_f32_32x32x2_f32 a[0:15], v38, v70, a[0:15]
	global_load_dwordx4 v[134:137], v[184:185], off offset:640
	global_load_dwordx4 v[150:153], v[186:187], off offset:640
	v_add_f32_e32 v41, v41, v57
	v_mul_f32_e32 v41, 0.5, v41
	s_waitcnt vmcnt(40)
	v_mfma_f32_32x32x2_f32 a[0:15], v39, v71, a[0:15]
	global_load_dwordx4 v[138:141], v[184:185], off offset:672
	global_load_dwordx4 v[154:157], v[186:187], off offset:672
	v_add_f32_e32 v42, v42, v58
	v_mul_f32_e32 v42, 0.5, v42
	s_waitcnt vmcnt(41)
	v_mfma_f32_32x32x2_f32 a[0:15], v40, v72, a[0:15]
	global_load_dwordx4 v[142:145], v[184:185], off offset:704
	global_load_dwordx4 v[158:161], v[186:187], off offset:704
	v_add_f32_e32 v43, v43, v59
	v_mul_f32_e32 v43, 0.5, v43
	s_waitcnt vmcnt(42)
	v_mfma_f32_32x32x2_f32 a[0:15], v41, v73, a[0:15]
	global_load_dwordx4 v[146:149], v[184:185], off offset:736
	global_load_dwordx4 v[162:165], v[186:187], off offset:736
	v_add_f32_e32 v44, v44, v60
	v_mul_f32_e32 v44, 0.5, v44
	s_waitcnt vmcnt(43)
	v_mfma_f32_32x32x2_f32 a[0:15], v42, v74, a[0:15]
	v_lshl_add_u64 v[188:189], v[16:17], 0, s[30:31]
	global_load_dword v166, v[188:189], off offset:-4096
	global_load_dword v167, v[188:189], off offset:-2048
	v_add_f32_e32 v45, v45, v61
	v_mul_f32_e32 v45, 0.5, v45
	s_waitcnt vmcnt(44)
	v_mfma_f32_32x32x2_f32 a[0:15], v43, v75, a[0:15]
	global_load_dword v168, v[188:189], off offset:0
	global_load_dword v169, v[188:189], off offset:2048
	v_add_f32_e32 v46, v46, v62
	v_mul_f32_e32 v46, 0.5, v46
	s_waitcnt vmcnt(45)
	v_mfma_f32_32x32x2_f32 a[0:15], v44, v76, a[0:15]
	v_lshl_add_u64 v[188:189], v[20:21], 0, s[30:31]
	global_load_dword v170, v[188:189], off offset:-4096
	global_load_dword v171, v[188:189], off offset:-2048
	v_add_f32_e32 v47, v47, v63
	v_mul_f32_e32 v47, 0.5, v47
	s_waitcnt vmcnt(46)
	v_mfma_f32_32x32x2_f32 a[0:15], v45, v77, a[0:15]
	global_load_dword v172, v[188:189], off offset:0
	global_load_dword v173, v[188:189], off offset:2048
	v_add_f32_e32 v48, v48, v64
	v_mul_f32_e32 v48, 0.5, v48
	s_waitcnt vmcnt(47)
	v_mfma_f32_32x32x2_f32 a[0:15], v46, v78, a[0:15]
	v_lshl_add_u64 v[188:189], v[18:19], 0, s[30:31]
	global_load_dword v174, v[188:189], off offset:-4096
	global_load_dword v175, v[188:189], off offset:-2048
	v_add_f32_e32 v49, v49, v65
	v_mul_f32_e32 v49, 0.5, v49
	s_waitcnt vmcnt(48)
	v_mfma_f32_32x32x2_f32 a[0:15], v47, v79, a[0:15]
	global_load_dword v176, v[188:189], off offset:0
	global_load_dword v177, v[188:189], off offset:2048
	v_add_f32_e32 v50, v50, v66
	v_mul_f32_e32 v50, 0.5, v50
	s_waitcnt vmcnt(49)
	v_mfma_f32_32x32x2_f32 a[0:15], v48, v80, a[0:15]
	v_lshl_add_u64 v[188:189], v[14:15], 0, s[30:31]
	global_load_dword v178, v[188:189], off offset:-4096
	global_load_dword v179, v[188:189], off offset:-2048
	v_add_f32_e32 v51, v51, v67
	v_mul_f32_e32 v51, 0.5, v51
	s_waitcnt vmcnt(50)
	v_mfma_f32_32x32x2_f32 a[0:15], v49, v81, a[0:15]
	global_load_dword v180, v[188:189], off offset:0
	global_load_dword v181, v[188:189], off offset:2048
	v_add_f32_e32 v52, v52, v68
	v_mul_f32_e32 v52, 0.5, v52
	s_waitcnt vmcnt(51)
	v_mfma_f32_32x32x2_f32 a[0:15], v50, v82, a[0:15]
	v_add_f32_e32 v53, v53, v69
	v_mul_f32_e32 v53, 0.5, v53
	s_waitcnt vmcnt(50)
	v_mfma_f32_32x32x2_f32 a[0:15], v51, v83, a[0:15]
	s_waitcnt vmcnt(49)
	v_mfma_f32_32x32x2_f32 a[0:15], v52, v84, a[0:15]
	s_waitcnt vmcnt(48)
	v_mfma_f32_32x32x2_f32 a[0:15], v53, v85, a[0:15]
	s_mov_b32 s30, 0x61000
	s_waitcnt vmcnt(46)
	v_add_f32_e32 v86, v86, v102
	v_mul_f32_e32 v86, 0.5, v86
	v_add_f32_e32 v87, v87, v103
	v_mul_f32_e32 v87, 0.5, v87
	v_add_f32_e32 v88, v88, v104
	v_mul_f32_e32 v88, 0.5, v88
	s_waitcnt vmcnt(39)
	v_mfma_f32_32x32x2_f32 a[0:15], v86, v118, a[0:15]
	global_load_dwordx4 v[38:41], v[184:185], off offset:768
	global_load_dwordx4 v[54:57], v[186:187], off offset:768
	v_add_f32_e32 v89, v89, v105
	v_mul_f32_e32 v89, 0.5, v89
	s_waitcnt vmcnt(40)
	v_mfma_f32_32x32x2_f32 a[0:15], v87, v119, a[0:15]
	global_load_dwordx4 v[42:45], v[184:185], off offset:800
	global_load_dwordx4 v[58:61], v[186:187], off offset:800
	v_add_f32_e32 v90, v90, v106
	v_mul_f32_e32 v90, 0.5, v90
	s_waitcnt vmcnt(41)
	v_mfma_f32_32x32x2_f32 a[0:15], v88, v120, a[0:15]
	global_load_dwordx4 v[46:49], v[184:185], off offset:832
	global_load_dwordx4 v[62:65], v[186:187], off offset:832
	v_add_f32_e32 v91, v91, v107
	v_mul_f32_e32 v91, 0.5, v91
	s_waitcnt vmcnt(42)
	v_mfma_f32_32x32x2_f32 a[0:15], v89, v121, a[0:15]
	global_load_dwordx4 v[50:53], v[184:185], off offset:864
	global_load_dwordx4 v[66:69], v[186:187], off offset:864
	v_add_f32_e32 v92, v92, v108
	v_mul_f32_e32 v92, 0.5, v92
	s_waitcnt vmcnt(43)
	v_mfma_f32_32x32x2_f32 a[0:15], v90, v122, a[0:15]
	v_lshl_add_u64 v[188:189], v[16:17], 0, s[30:31]
	global_load_dword v70, v[188:189], off offset:-4096
	global_load_dword v71, v[188:189], off offset:-2048
	v_add_f32_e32 v93, v93, v109
	v_mul_f32_e32 v93, 0.5, v93
	s_waitcnt vmcnt(44)
	v_mfma_f32_32x32x2_f32 a[0:15], v91, v123, a[0:15]
	global_load_dword v72, v[188:189], off offset:0
	global_load_dword v73, v[188:189], off offset:2048
	v_add_f32_e32 v94, v94, v110
	v_mul_f32_e32 v94, 0.5, v94
	s_waitcnt vmcnt(45)
	v_mfma_f32_32x32x2_f32 a[0:15], v92, v124, a[0:15]
	v_lshl_add_u64 v[188:189], v[20:21], 0, s[30:31]
	global_load_dword v74, v[188:189], off offset:-4096
	global_load_dword v75, v[188:189], off offset:-2048
	v_add_f32_e32 v95, v95, v111
	v_mul_f32_e32 v95, 0.5, v95
	s_waitcnt vmcnt(46)
	v_mfma_f32_32x32x2_f32 a[0:15], v93, v125, a[0:15]
	global_load_dword v76, v[188:189], off offset:0
	global_load_dword v77, v[188:189], off offset:2048
	v_add_f32_e32 v96, v96, v112
	v_mul_f32_e32 v96, 0.5, v96
	s_waitcnt vmcnt(47)
	v_mfma_f32_32x32x2_f32 a[0:15], v94, v126, a[0:15]
	v_lshl_add_u64 v[188:189], v[18:19], 0, s[30:31]
	global_load_dword v78, v[188:189], off offset:-4096
	global_load_dword v79, v[188:189], off offset:-2048
	v_add_f32_e32 v97, v97, v113
	v_mul_f32_e32 v97, 0.5, v97
	s_waitcnt vmcnt(48)
	v_mfma_f32_32x32x2_f32 a[0:15], v95, v127, a[0:15]
	global_load_dword v80, v[188:189], off offset:0
	global_load_dword v81, v[188:189], off offset:2048
	v_add_f32_e32 v98, v98, v114
	v_mul_f32_e32 v98, 0.5, v98
	s_waitcnt vmcnt(49)
	v_mfma_f32_32x32x2_f32 a[0:15], v96, v128, a[0:15]
	v_lshl_add_u64 v[188:189], v[14:15], 0, s[30:31]
	global_load_dword v82, v[188:189], off offset:-4096
	global_load_dword v83, v[188:189], off offset:-2048
	v_add_f32_e32 v99, v99, v115
	v_mul_f32_e32 v99, 0.5, v99
	s_waitcnt vmcnt(50)
	v_mfma_f32_32x32x2_f32 a[0:15], v97, v129, a[0:15]
	global_load_dword v84, v[188:189], off offset:0
	global_load_dword v85, v[188:189], off offset:2048
	v_add_f32_e32 v100, v100, v116
	v_mul_f32_e32 v100, 0.5, v100
	s_waitcnt vmcnt(51)
	v_mfma_f32_32x32x2_f32 a[0:15], v98, v130, a[0:15]
	v_add_f32_e32 v101, v101, v117
	v_mul_f32_e32 v101, 0.5, v101
	s_waitcnt vmcnt(50)
	v_mfma_f32_32x32x2_f32 a[0:15], v99, v131, a[0:15]
	s_waitcnt vmcnt(49)
	v_mfma_f32_32x32x2_f32 a[0:15], v100, v132, a[0:15]
	s_waitcnt vmcnt(48)
	v_mfma_f32_32x32x2_f32 a[0:15], v101, v133, a[0:15]
	s_mov_b32 s30, 0x71000
	s_waitcnt vmcnt(46)
	v_add_f32_e32 v134, v134, v150
	v_mul_f32_e32 v134, 0.5, v134
	v_add_f32_e32 v135, v135, v151
	v_mul_f32_e32 v135, 0.5, v135
	v_add_f32_e32 v136, v136, v152
	v_mul_f32_e32 v136, 0.5, v136
	s_waitcnt vmcnt(39)
	v_mfma_f32_32x32x2_f32 a[0:15], v134, v166, a[0:15]
	global_load_dwordx4 v[86:89], v[184:185], off offset:896
	global_load_dwordx4 v[102:105], v[186:187], off offset:896
	v_add_f32_e32 v137, v137, v153
	v_mul_f32_e32 v137, 0.5, v137
	s_waitcnt vmcnt(40)
	v_mfma_f32_32x32x2_f32 a[0:15], v135, v167, a[0:15]
	global_load_dwordx4 v[90:93], v[184:185], off offset:928
	global_load_dwordx4 v[106:109], v[186:187], off offset:928
	v_add_f32_e32 v138, v138, v154
	v_mul_f32_e32 v138, 0.5, v138
	s_waitcnt vmcnt(41)
	v_mfma_f32_32x32x2_f32 a[0:15], v136, v168, a[0:15]
	global_load_dwordx4 v[94:97], v[184:185], off offset:960
	global_load_dwordx4 v[110:113], v[186:187], off offset:960
	v_add_f32_e32 v139, v139, v155
	v_mul_f32_e32 v139, 0.5, v139
	s_waitcnt vmcnt(42)
	v_mfma_f32_32x32x2_f32 a[0:15], v137, v169, a[0:15]
	global_load_dwordx4 v[98:101], v[184:185], off offset:992
	global_load_dwordx4 v[114:117], v[186:187], off offset:992
	v_add_f32_e32 v140, v140, v156
	v_mul_f32_e32 v140, 0.5, v140
	s_waitcnt vmcnt(43)
	v_mfma_f32_32x32x2_f32 a[0:15], v138, v170, a[0:15]
	v_lshl_add_u64 v[188:189], v[16:17], 0, s[30:31]
	global_load_dword v118, v[188:189], off offset:-4096
	global_load_dword v119, v[188:189], off offset:-2048
	v_add_f32_e32 v141, v141, v157
	v_mul_f32_e32 v141, 0.5, v141
	s_waitcnt vmcnt(44)
	v_mfma_f32_32x32x2_f32 a[0:15], v139, v171, a[0:15]
	global_load_dword v120, v[188:189], off offset:0
	global_load_dword v121, v[188:189], off offset:2048
	v_add_f32_e32 v142, v142, v158
	v_mul_f32_e32 v142, 0.5, v142
	s_waitcnt vmcnt(45)
	v_mfma_f32_32x32x2_f32 a[0:15], v140, v172, a[0:15]
	v_lshl_add_u64 v[188:189], v[20:21], 0, s[30:31]
	global_load_dword v122, v[188:189], off offset:-4096
	global_load_dword v123, v[188:189], off offset:-2048
	v_add_f32_e32 v143, v143, v159
	v_mul_f32_e32 v143, 0.5, v143
	s_waitcnt vmcnt(46)
	v_mfma_f32_32x32x2_f32 a[0:15], v141, v173, a[0:15]
	global_load_dword v124, v[188:189], off offset:0
	global_load_dword v125, v[188:189], off offset:2048
	v_add_f32_e32 v144, v144, v160
	v_mul_f32_e32 v144, 0.5, v144
	s_waitcnt vmcnt(47)
	v_mfma_f32_32x32x2_f32 a[0:15], v142, v174, a[0:15]
	v_lshl_add_u64 v[188:189], v[18:19], 0, s[30:31]
	global_load_dword v126, v[188:189], off offset:-4096
	global_load_dword v127, v[188:189], off offset:-2048
	v_add_f32_e32 v145, v145, v161
	v_mul_f32_e32 v145, 0.5, v145
	s_waitcnt vmcnt(48)
	v_mfma_f32_32x32x2_f32 a[0:15], v143, v175, a[0:15]
	global_load_dword v128, v[188:189], off offset:0
	global_load_dword v129, v[188:189], off offset:2048
	v_add_f32_e32 v146, v146, v162
	v_mul_f32_e32 v146, 0.5, v146
	s_waitcnt vmcnt(49)
	v_mfma_f32_32x32x2_f32 a[0:15], v144, v176, a[0:15]
	v_lshl_add_u64 v[188:189], v[14:15], 0, s[30:31]
	global_load_dword v130, v[188:189], off offset:-4096
	global_load_dword v131, v[188:189], off offset:-2048
	v_add_f32_e32 v147, v147, v163
	v_mul_f32_e32 v147, 0.5, v147
	s_waitcnt vmcnt(50)
	v_mfma_f32_32x32x2_f32 a[0:15], v145, v177, a[0:15]
	global_load_dword v132, v[188:189], off offset:0
	global_load_dword v133, v[188:189], off offset:2048
	v_add_f32_e32 v148, v148, v164
	v_mul_f32_e32 v148, 0.5, v148
	s_waitcnt vmcnt(51)
	v_mfma_f32_32x32x2_f32 a[0:15], v146, v178, a[0:15]
	v_add_f32_e32 v149, v149, v165
	v_mul_f32_e32 v149, 0.5, v149
	s_waitcnt vmcnt(50)
	v_mfma_f32_32x32x2_f32 a[0:15], v147, v179, a[0:15]
	s_waitcnt vmcnt(49)
	v_mfma_f32_32x32x2_f32 a[0:15], v148, v180, a[0:15]
	s_waitcnt vmcnt(48)
	v_mfma_f32_32x32x2_f32 a[0:15], v149, v181, a[0:15]
	s_waitcnt vmcnt(46)
	v_add_f32_e32 v38, v38, v54
	v_mul_f32_e32 v38, 0.5, v38
	v_add_f32_e32 v39, v39, v55
	v_mul_f32_e32 v39, 0.5, v39
	v_add_f32_e32 v40, v40, v56
	v_mul_f32_e32 v40, 0.5, v40
	s_waitcnt vmcnt(39)
	v_mfma_f32_32x32x2_f32 a[0:15], v38, v70, a[0:15]
	v_add_f32_e32 v41, v41, v57
	v_mul_f32_e32 v41, 0.5, v41
	s_waitcnt vmcnt(38)
	v_mfma_f32_32x32x2_f32 a[0:15], v39, v71, a[0:15]
	v_add_f32_e32 v42, v42, v58
	v_mul_f32_e32 v42, 0.5, v42
	s_waitcnt vmcnt(37)
	v_mfma_f32_32x32x2_f32 a[0:15], v40, v72, a[0:15]
	v_add_f32_e32 v43, v43, v59
	v_mul_f32_e32 v43, 0.5, v43
	s_waitcnt vmcnt(36)
	v_mfma_f32_32x32x2_f32 a[0:15], v41, v73, a[0:15]
	v_add_f32_e32 v44, v44, v60
	v_mul_f32_e32 v44, 0.5, v44
	s_waitcnt vmcnt(35)
	v_mfma_f32_32x32x2_f32 a[0:15], v42, v74, a[0:15]
	v_add_f32_e32 v45, v45, v61
	v_mul_f32_e32 v45, 0.5, v45
	s_waitcnt vmcnt(34)
	v_mfma_f32_32x32x2_f32 a[0:15], v43, v75, a[0:15]
	v_add_f32_e32 v46, v46, v62
	v_mul_f32_e32 v46, 0.5, v46
	s_waitcnt vmcnt(33)
	v_mfma_f32_32x32x2_f32 a[0:15], v44, v76, a[0:15]
	v_add_f32_e32 v47, v47, v63
	v_mul_f32_e32 v47, 0.5, v47
	s_waitcnt vmcnt(32)
	v_mfma_f32_32x32x2_f32 a[0:15], v45, v77, a[0:15]
	v_add_f32_e32 v48, v48, v64
	v_mul_f32_e32 v48, 0.5, v48
	s_waitcnt vmcnt(31)
	v_mfma_f32_32x32x2_f32 a[0:15], v46, v78, a[0:15]
	v_add_f32_e32 v49, v49, v65
	v_mul_f32_e32 v49, 0.5, v49
	s_waitcnt vmcnt(30)
	v_mfma_f32_32x32x2_f32 a[0:15], v47, v79, a[0:15]
	v_add_f32_e32 v50, v50, v66
	v_mul_f32_e32 v50, 0.5, v50
	s_waitcnt vmcnt(29)
	v_mfma_f32_32x32x2_f32 a[0:15], v48, v80, a[0:15]
	v_add_f32_e32 v51, v51, v67
	v_mul_f32_e32 v51, 0.5, v51
	s_waitcnt vmcnt(28)
	v_mfma_f32_32x32x2_f32 a[0:15], v49, v81, a[0:15]
	v_add_f32_e32 v52, v52, v68
	v_mul_f32_e32 v52, 0.5, v52
	s_waitcnt vmcnt(27)
	v_mfma_f32_32x32x2_f32 a[0:15], v50, v82, a[0:15]
	v_add_f32_e32 v53, v53, v69
	v_mul_f32_e32 v53, 0.5, v53
	s_waitcnt vmcnt(26)
	v_mfma_f32_32x32x2_f32 a[0:15], v51, v83, a[0:15]
	s_waitcnt vmcnt(25)
	v_mfma_f32_32x32x2_f32 a[0:15], v52, v84, a[0:15]
	s_waitcnt vmcnt(24)
	v_mfma_f32_32x32x2_f32 a[0:15], v53, v85, a[0:15]
	s_waitcnt vmcnt(22)
	v_add_f32_e32 v86, v86, v102
	v_mul_f32_e32 v86, 0.5, v86
	v_add_f32_e32 v87, v87, v103
	v_mul_f32_e32 v87, 0.5, v87
	v_add_f32_e32 v88, v88, v104
	v_mul_f32_e32 v88, 0.5, v88
	s_waitcnt vmcnt(15)
	v_mfma_f32_32x32x2_f32 a[0:15], v86, v118, a[0:15]
	v_add_f32_e32 v89, v89, v105
	v_mul_f32_e32 v89, 0.5, v89
	s_waitcnt vmcnt(14)
	v_mfma_f32_32x32x2_f32 a[0:15], v87, v119, a[0:15]
	v_add_f32_e32 v90, v90, v106
	v_mul_f32_e32 v90, 0.5, v90
	s_waitcnt vmcnt(13)
	v_mfma_f32_32x32x2_f32 a[0:15], v88, v120, a[0:15]
	v_add_f32_e32 v91, v91, v107
	v_mul_f32_e32 v91, 0.5, v91
	s_waitcnt vmcnt(12)
	v_mfma_f32_32x32x2_f32 a[0:15], v89, v121, a[0:15]
	v_add_f32_e32 v92, v92, v108
	v_mul_f32_e32 v92, 0.5, v92
	s_waitcnt vmcnt(11)
	v_mfma_f32_32x32x2_f32 a[0:15], v90, v122, a[0:15]
	v_add_f32_e32 v93, v93, v109
	v_mul_f32_e32 v93, 0.5, v93
	s_waitcnt vmcnt(10)
	v_mfma_f32_32x32x2_f32 a[0:15], v91, v123, a[0:15]
	v_add_f32_e32 v94, v94, v110
	v_mul_f32_e32 v94, 0.5, v94
	s_waitcnt vmcnt(9)
	v_mfma_f32_32x32x2_f32 a[0:15], v92, v124, a[0:15]
	v_add_f32_e32 v95, v95, v111
	v_mul_f32_e32 v95, 0.5, v95
	s_waitcnt vmcnt(8)
	v_mfma_f32_32x32x2_f32 a[0:15], v93, v125, a[0:15]
	v_add_f32_e32 v96, v96, v112
	v_mul_f32_e32 v96, 0.5, v96
	s_waitcnt vmcnt(7)
	v_mfma_f32_32x32x2_f32 a[0:15], v94, v126, a[0:15]
	v_add_f32_e32 v97, v97, v113
	v_mul_f32_e32 v97, 0.5, v97
	s_waitcnt vmcnt(6)
	v_mfma_f32_32x32x2_f32 a[0:15], v95, v127, a[0:15]
	v_add_f32_e32 v98, v98, v114
	v_mul_f32_e32 v98, 0.5, v98
	s_waitcnt vmcnt(5)
	v_mfma_f32_32x32x2_f32 a[0:15], v96, v128, a[0:15]
	v_add_f32_e32 v99, v99, v115
	v_mul_f32_e32 v99, 0.5, v99
	s_waitcnt vmcnt(4)
	v_mfma_f32_32x32x2_f32 a[0:15], v97, v129, a[0:15]
	v_add_f32_e32 v100, v100, v116
	v_mul_f32_e32 v100, 0.5, v100
	s_waitcnt vmcnt(3)
	v_mfma_f32_32x32x2_f32 a[0:15], v98, v130, a[0:15]
	v_add_f32_e32 v101, v101, v117
	v_mul_f32_e32 v101, 0.5, v101
	s_waitcnt vmcnt(2)
	v_mfma_f32_32x32x2_f32 a[0:15], v99, v131, a[0:15]
	s_waitcnt vmcnt(1)
	v_mfma_f32_32x32x2_f32 a[0:15], v100, v132, a[0:15]
	s_waitcnt vmcnt(0)
	v_mfma_f32_32x32x2_f32 a[0:15], v101, v133, a[0:15]
	s_mov_b32 s30, 0x80000
	s_mov_b32 s31, 0
	s_nop 1
	s_lshl_b32 s28, s34, 5
	s_and_b32 s28, s28, 0x1e0
	v_or_b32_e32 v14, s28, v2
	v_lshlrev_b32_e32 v14, 2, v14
	s_nop 12
	ds_write_b32 v3, a0
	ds_write_b32 v3, a1 offset:256
	ds_write_b32 v3, a2 offset:512
	ds_write_b32 v3, a3 offset:768
	ds_write_b32 v3, a4 offset:1024
	ds_write_b32 v3, a5 offset:1280
	ds_write_b32 v3, a6 offset:1536
	ds_write_b32 v3, a7 offset:1792
	ds_write_b32 v3, a8 offset:2048
	ds_write_b32 v3, a9 offset:2304
	ds_write_b32 v3, a10 offset:2560
	ds_write_b32 v3, a11 offset:2816
	ds_write_b32 v3, a12 offset:3072
	ds_write_b32 v3, a13 offset:3328
	ds_write_b32 v3, a14 offset:3584
	ds_write_b32 v3, a15 offset:3840
	s_waitcnt lgkmcnt(0)
	s_barrier
	global_load_dword v37, v14, s[22:23]
	global_load_dword v42, v14, s[26:27]
	ds_read2st64_b32 v[14:15], v28 offset1:4
	ds_read2st64_b32 v[16:17], v28 offset0:16 offset1:20
	ds_read2st64_b32 v[18:19], v28 offset0:32 offset1:36
	ds_read2st64_b32 v[20:21], v28 offset0:48 offset1:52
	ds_read2st64_b32 v[22:23], v28 offset0:8 offset1:12
	ds_read2st64_b32 v[24:25], v28 offset0:24 offset1:28
	ds_read2st64_b32 v[38:39], v28 offset0:40 offset1:44
	ds_read2st64_b32 v[40:41], v28 offset0:56 offset1:60
	s_waitcnt lgkmcnt(6)
	v_add_f32_e32 v14, v14, v16
	v_add_f32_e32 v15, v15, v17
	s_waitcnt lgkmcnt(5)
	v_add_f32_e32 v14, v14, v18
	s_waitcnt lgkmcnt(2)
	v_add_f32_e32 v16, v22, v24
	v_add_f32_e32 v15, v15, v19
	v_add_f32_e32 v14, v14, v20
	v_add_f32_e32 v17, v23, v25
	s_waitcnt lgkmcnt(1)
	v_add_f32_e32 v16, v16, v38
	v_add_f32_e32 v15, v15, v21
	v_add_f32_e32 v17, v17, v39
	s_waitcnt lgkmcnt(0)
	v_add_f32_e32 v16, v16, v40
	v_add_f32_e32 v17, v17, v41
	v_cmp_lt_i32_e32 vcc, v31, v30
	s_waitcnt vmcnt(1)
	v_add_f32_e32 v14, v14, v37
	v_add_f32_e32 v15, v15, v37
	v_max_f32_e32 v14, 0, v14
	v_add_f32_e32 v16, v16, v37
	v_max_f32_e32 v15, 0, v15
	s_waitcnt vmcnt(0)
	v_fma_f32 v14, v42, v14, 0
	v_add_f32_e32 v17, v17, v37
	v_max_f32_e32 v16, 0, v16
	v_fmac_f32_e32 v14, v42, v15
	v_cndmask_b32_e32 v43, v29, v31, vcc
	v_max_f32_e32 v17, 0, v17
	v_fmac_f32_e32 v14, v42, v16
	v_lshlrev_b32_e32 v43, 2, v43
	v_fmac_f32_e32 v14, v42, v17
	ds_bpermute_b32 v15, v43, v14
	v_cmp_lt_i32_e32 vcc, v32, v30
	s_waitcnt lgkmcnt(0)
	v_add_f32_e32 v14, v14, v15
	v_cndmask_b32_e32 v16, v29, v32, vcc
	v_lshlrev_b32_e32 v16, 2, v16
	ds_bpermute_b32 v15, v16, v14
	v_cmp_lt_i32_e32 vcc, v33, v30
	s_waitcnt lgkmcnt(0)
	v_add_f32_e32 v14, v14, v15
	v_cndmask_b32_e32 v16, v29, v33, vcc
	v_lshlrev_b32_e32 v16, 2, v16
	ds_bpermute_b32 v15, v16, v14
	v_cmp_lt_i32_e32 vcc, v34, v30
	s_waitcnt lgkmcnt(0)
	v_add_f32_e32 v14, v14, v15
	v_cndmask_b32_e32 v16, v29, v34, vcc
	v_lshlrev_b32_e32 v16, 2, v16
	ds_bpermute_b32 v15, v16, v14
	v_cmp_lt_i32_e32 vcc, v35, v30
	s_waitcnt lgkmcnt(0)
	v_add_f32_e32 v14, v14, v15
	v_cndmask_b32_e32 v16, v29, v35, vcc
	v_lshlrev_b32_e32 v16, 2, v16
	ds_bpermute_b32 v15, v16, v14
	v_cmp_lt_i32_e32 vcc, v36, v30
	s_waitcnt lgkmcnt(0)
	v_add_f32_e32 v14, v14, v15
	v_cndmask_b32_e32 v16, v29, v36, vcc
	v_lshlrev_b32_e32 v15, 2, v16
	ds_bpermute_b32 v15, v15, v14
	s_and_saveexec_b64 s[30:31], s[8:9]
	s_cbranch_execz .LBB2_18
	s_waitcnt lgkmcnt(0)
	v_add_f32_e32 v14, v14, v15
	ds_write_b32 v27, v14
.LBB2_18:
	s_or_b64 exec, exec, s[30:31]
	s_waitcnt lgkmcnt(0)
	s_barrier
	s_and_saveexec_b64 s[30:31], s[6:7]
	s_cbranch_execz .LBB2_5
	ds_read_b128 v[14:17], v1 offset:16384
	s_or_b32 s28, s39, s37
	s_lshl_b64 s[42:43], s[28:29], 7
	s_add_u32 s42, s16, s42
	s_addc_u32 s43, s17, s43
	s_waitcnt lgkmcnt(0)
	v_add_f32_e32 v14, v14, v15
	v_add_f32_e32 v14, v14, v16
	s_lshl_b32 s28, s36, 2
	s_mov_b64 s[34:35], exec
	v_add_f32_e32 v14, v14, v17
	v_mov_b32_e32 v15, s28
	global_store_dword v15, v14, s[42:43] sc0 sc1
	v_mbcnt_lo_u32_b32 v14, s34, 0
	s_waitcnt vmcnt(0)
	s_waitcnt vmcnt(0)
	v_mbcnt_hi_u32_b32 v14, s35, v14
	v_cmp_eq_u32_e32 vcc, 0, v14
	s_and_b64 s[36:37], exec, vcc
	s_mov_b64 exec, s[36:37]
	s_cbranch_execz .LBB2_5
	s_bcnt1_i32_b64 s28, s[34:35]
	v_mov_b32_e32 v14, s28
	global_atomic_add v1, v14, s[18:19] offset:32
	s_branch .LBB2_5

	.amdhsa_kernel _Z20refine_gather_kernelPKfS0_S0_S0_S0_S0_S0_PfPiS1_
		.amdhsa_group_segment_fixed_size 16424
		.amdhsa_private_segment_fixed_size 0
		.amdhsa_kernarg_size 80
		.amdhsa_user_sgpr_count 2
		.amdhsa_user_sgpr_dispatch_ptr 0
		.amdhsa_user_sgpr_queue_ptr 0
		.amdhsa_user_sgpr_kernarg_segment_ptr 1
		.amdhsa_user_sgpr_dispatch_id 0
		.amdhsa_user_sgpr_kernarg_preload_length 0
		.amdhsa_user_sgpr_kernarg_preload_offset 0
		.amdhsa_user_sgpr_private_segment_size 0
		.amdhsa_uses_dynamic_stack 0
		.amdhsa_enable_private_segment 0
		.amdhsa_system_sgpr_workgroup_id_x 1
		.amdhsa_system_sgpr_workgroup_id_y 0
		.amdhsa_system_sgpr_workgroup_id_z 0
		.amdhsa_system_sgpr_workgroup_info 0
		.amdhsa_system_vgpr_workitem_id 0
		.amdhsa_next_free_vgpr 208
		.amdhsa_next_free_sgpr 100
		.amdhsa_accum_offset 192
		.amdhsa_reserve_vcc 1
		.amdhsa_float_round_mode_32 0
		.amdhsa_float_round_mode_16_64 0
		.amdhsa_float_denorm_mode_32 3
		.amdhsa_float_denorm_mode_16_64 3
		.amdhsa_dx10_clamp 1
		.amdhsa_ieee_mode 1
		.amdhsa_fp16_overflow 0
		.amdhsa_tg_split 0
		.amdhsa_exception_fp_ieee_invalid_op 0
		.amdhsa_exception_fp_denorm_src 0
		.amdhsa_exception_fp_ieee_div_zero 0
		.amdhsa_exception_fp_ieee_overflow 0
		.amdhsa_exception_fp_ieee_underflow 0
		.amdhsa_exception_fp_ieee_inexact 0
		.amdhsa_exception_int_div_zero 0
	.end_amdhsa_kernel

amdhsa.kernels:
  - .agpr_count:     0
    .args:
      - .actual_access:  read_only
        .address_space:  global
        .offset:         0
        .size:           8
        .value_kind:     global_buffer
      - .actual_access:  write_only
        .address_space:  global
        .offset:         8
        .size:           8
        .value_kind:     global_buffer
    .group_segment_fixed_size: 0
    .kernarg_segment_align: 8
    .kernarg_segment_size: 16
    .language:       OpenCL C
    .language_version:
      - 2
      - 0
    .max_flat_workgroup_size: 256
    .name:           _Z7prep_w1PKfPDv8_DF16_
    .private_segment_fixed_size: 0
    .sgpr_count:     14
    .sgpr_spill_count: 0
    .symbol:         _Z7prep_w1PKfPDv8_DF16_.kd
    .uniform_work_group_size: 1
    .uses_dynamic_stack: false
    .vgpr_count:     26
    .vgpr_spill_count: 0
    .wavefront_size: 64
  - .agpr_count:     0
    .args:
      - .address_space:  global
        .offset:         0
        .size:           8
        .value_kind:     global_buffer
      - .address_space:  global
        .offset:         8
        .size:           8
        .value_kind:     global_buffer
      - .address_space:  global
        .offset:         16
        .size:           8
        .value_kind:     global_buffer
      - .actual_access:  read_only
        .address_space:  global
        .offset:         24
        .size:           8
        .value_kind:     global_buffer
      - .actual_access:  read_only
        .address_space:  global
        .offset:         32
        .size:           8
        .value_kind:     global_buffer
      - .actual_access:  write_only
        .address_space:  global
        .offset:         40
        .size:           8
        .value_kind:     global_buffer
      - .actual_access:  write_only
        .address_space:  global
        .offset:         48
        .size:           8
        .value_kind:     global_buffer
    .group_segment_fixed_size: 163840
    .kernarg_segment_align: 8
    .kernarg_segment_size: 56
    .language:       OpenCL C
    .language_version:
      - 2
      - 0
    .max_flat_workgroup_size: 768
    .name:           _Z12score_kernelPKfS0_PKcS0_S0_PfPi
    .private_segment_fixed_size: 0
    .sgpr_count:     34
    .sgpr_spill_count: 0
    .symbol:         _Z12score_kernelPKfS0_PKcS0_S0_PfPi.kd
    .uniform_work_group_size: 1
    .uses_dynamic_stack: false
    .vgpr_count:     164
    .vgpr_spill_count: 0
    .wavefront_size: 64
  - .agpr_count:     16
    .args:
      - .actual_access:  read_only
        .address_space:  global
        .offset:         0
        .size:           8
        .value_kind:     global_buffer
      - .actual_access:  read_only
        .address_space:  global
        .offset:         8
        .size:           8
        .value_kind:     global_buffer
      - .actual_access:  read_only
        .address_space:  global
        .offset:         16
        .size:           8
        .value_kind:     global_buffer
      - .actual_access:  read_only
        .address_space:  global
        .offset:         24
        .size:           8
        .value_kind:     global_buffer
      - .actual_access:  read_only
        .address_space:  global
        .offset:         32
        .size:           8
        .value_kind:     global_buffer
      - .actual_access:  read_only
        .address_space:  global
        .offset:         40
        .size:           8
        .value_kind:     global_buffer
      - .actual_access:  read_only
        .address_space:  global
        .offset:         48
        .size:           8
        .value_kind:     global_buffer
      - .address_space:  global
        .offset:         56
        .size:           8
        .value_kind:     global_buffer
      - .address_space:  global
        .offset:         64
        .size:           8
        .value_kind:     global_buffer
      - .actual_access:  write_only
        .address_space:  global
        .offset:         72
        .size:           8
        .value_kind:     global_buffer
    .group_segment_fixed_size: 16424
    .kernarg_segment_align: 8
    .kernarg_segment_size: 80
    .language:       OpenCL C
    .language_version:
      - 2
      - 0
    .max_flat_workgroup_size: 256
    .name:           _Z20refine_gather_kernelPKfS0_S0_S0_S0_S0_S0_PfPiS1_
    .private_segment_fixed_size: 0
    .sgpr_count:     106
    .sgpr_spill_count: 94
    .symbol:         _Z20refine_gather_kernelPKfS0_S0_S0_S0_S0_S0_PfPiS1_.kd
    .uniform_work_group_size: 1
    .uses_dynamic_stack: false
    .vgpr_count:     208
    .vgpr_spill_count: 0
    .wavefront_size: 64
